# attention tile loops: wave-uniform active test branches on SCC / mask bit instead of cndmask+readfirstlane+bitcmp
# baseline (speedup 1.0000x reference)
; template <bool MLA>
; __device__ __forceinline__ void attn_unit(char* lds, int h, int qb, const bf16_t* Qp, int ldq, const bf16_t* Kp, int ldk, const bf16_t* KRp, const bf16_t* Vp, int ldv,
;                                           unsigned char* Op, int ldo, const float* KMp, const float* rel_bias) {
;     ...
;         if (t + 1 < NT) A_ISSUE(kb + 64, buf ^ 1);
;         int act;
;         if (MLA || jb == qb) act = (kb <= qlo + 31) ? 1 : 0; else act = __any((int)((mysel >> jb) & 1u)) ? 1 : 0;
;         act = __builtin_amdgcn_readfirstlane(act);
;         if (act) {
;             f32x16 p0, p1;
; #pragma unroll
;             for (int r = 0; r < 16; ++r) { p0[r] = 0.f; p1[r] = 0.f; }
;             { const char* kn = lds + buf * SHM_KN; const char* kr = lds + buf * SHM_KR;
; #pragma unroll
;               for (int d0 = 0; d0 < 8; ++d0) { const char* ap = kn + kan[d0 & 3] + (d0 >> 2) * 128;
;                   const bf16x8 a0 = *(const bf16x8*)ap, a1 = *(const bf16x8*)(ap + 32 * 256);
;                   p0 = __builtin_amdgcn_mfma_f32_32x32x16_bf16(a0, qr[d0], p0, 0, 0, 0);
;                   p1 = __builtin_amdgcn_mfma_f32_32x32x16_bf16(a1, qr[d0], p1, 0, 0, 0); }
.LBB0_1388:
	s_sub_i32 s22, s10, 64
	s_cmp_le_u32 s22, s51
	s_cbranch_scc0 .Lmla_inact
	s_lshl_b32 s53, s46, 14
	s_add_i32 s22, s53, 0
	v_add3_u32 v70, s22, v154, v153
	ds_read_b128 v[66:69], v70 offset:32768
	ds_read_b128 v[180:183], v70 offset:32896
	v_add3_u32 v179, s22, v155, v153
	s_lshl_b32 s23, s46, 13
	s_waitcnt lgkmcnt(0)
	v_mfma_f32_32x32x16_bf16 v[82:97], v[66:69], v[98:101], 0
	s_cmp_lt_u32 s52, s50
	s_cselect_b32 s101, 1, 0
	s_cbranch_scc0 .Lmla_nk0
	s_lshl_b64 s[98:99], s[10:11], 12
	s_add_u32 s98, s44, s98
	s_addc_u32 s99, s45, s99
	s_lshl_b32 s100, s46, 14
	s_xor_b32 s100, s100, 0x4000
	s_add_i32 s100, s48, s100
	s_add_i32 m0, s100, 0x8000
	v_lshl_add_u64 v[228:229], v[146:147], 1, s[98:99]
	global_load_lds_dwordx4 v176, s[98:99]

; template <bool MLA>
; __device__ __forceinline__ void attn_unit(char* lds, int h, int qb, const bf16_t* Qp, int ldq, const bf16_t* Kp, int ldk, const bf16_t* KRp, const bf16_t* Vp, int ldv,
;                                           unsigned char* Op, int ldo, const float* KMp, const float* rel_bias) {
;     ...
;         if (MLA || jb == qb) act = (kb <= qlo + 31) ? 1 : 0; else act = __any((int)((mysel >> jb) & 1u)) ? 1 : 0;
;         act = __builtin_amdgcn_readfirstlane(act);
;         if (act) {
;             f32x16 p0, p1;
; #pragma unroll
;             for (int r = 0; r < 16; ++r) { p0[r] = 0.f; p1[r] = 0.f; }
;             { const char* kn = lds + buf * SHM_KN; const char* kr = lds + buf * SHM_KR;
; #pragma unroll
;               for (int d0 = 0; d0 < 8; ++d0) { const char* ap = kn + kan[d0 & 3] + (d0 >> 2) * 128;
;                   const bf16x8 a0 = *(const bf16x8*)ap, a1 = *(const bf16x8*)(ap + 32 * 256);
;                   p0 = __builtin_amdgcn_mfma_f32_32x32x16_bf16(a0, qr[d0], p0, 0, 0, 0);
;                   p1 = __builtin_amdgcn_mfma_f32_32x32x16_bf16(a1, qr[d0], p1, 0, 0, 0); }
;               if constexpr (MLA) {
; #pragma unroll
;                   for (int d0 = 8; d0 < 12; ++d0) { const char* ap = kr + kar[d0 & 3];
;                       const bf16x8 a0 = *(const bf16x8*)ap, a1 = *(const bf16x8*)(ap + 32 * 128);
;                       p0 = __builtin_amdgcn_mfma_f32_32x32x16_bf16(a0, qr[d0], p0, 0, 0, 0);
;                       p1 = __builtin_amdgcn_mfma_f32_32x32x16_bf16(a1, qr[d0], p1, 0, 0, 0); } } }
;             const int dq = qpos - kb - 4 * hi;
;             if constexpr (MLA) {
;                 if (kb + 63 > qlo) {
; #pragma unroll
;                     for (int r = 0; r < 16; ++r) { const int d0 = dq - CROWC(r); if (d0 < 0) p0[r] = NEG; if (d0 < 32) p1[r] = NEG; } }
;             } else {
;                 const bool selq = (jb == qb) || (((mysel >> jb) & 1u) != 0u);
;                 if (q0 - (kb + 63) >= 128) { const float cb = bt_l[128];
; #pragma unroll
;                     for (int r = 0; r < 16; ++r) { p0[r] = selq ? p0[r] + cb : NEG; p1[r] = selq ? p1[r] + cb : NEG; } }
;                 else {
; #pragma unroll
;                     for (int r4 = 0; r4 < 4; ++r4) {
; #pragma unroll
;                         for (int rr = 0; rr < 4; ++rr) { const int r = r4 * 4 + rr; const int d0 = dq - CROWC(r), d1 = d0 - 32;
.LBB0_1559:
	s_bitcmp0_b32 s54, 0
	s_cbranch_scc1 .Lmoba_inact
	s_add_i32 s22, s75, 0
	v_add_u32_e32 v2, s22, v203
	ds_read_b128 v[68:71], v2 offset:32768
	ds_read_b128 v[72:75], v2 offset:32896
	s_mov_b64 s[54:55], -1
	s_waitcnt lgkmcnt(0)
	v_mfma_f32_32x32x16_bf16 v[100:115], v[68:71], v[160:163], 0
	s_xor_b32 s100, s75, 0x4000
	s_add_i32 s100, s27, s100
	v_lshl_add_u64 v[228:229], s[52:53], 0, v[182:183]
	s_add_i32 m0, s100, 0x8000
	s_nop 0
	global_load_lds_dwordx4 v[228:229], off
	ds_read_b128 v[68:71], v2 offset:40960
	ds_read_b128 v[76:79], v2 offset:41088
	v_add_u32_e32 v2, s22, v204
	s_waitcnt lgkmcnt(0)
	v_mfma_f32_32x32x16_bf16 v[84:99], v[68:71], v[160:163], 0
	v_lshl_add_u64 v[228:229], s[52:53], 0, v[180:181]
	v_lshl_add_u64 v[230:231], v[228:229], 0, s[46:47]
	s_mov_b32 m0, s100
	v_lshl_add_u64 v[228:229], v[228:229], 0, s[48:49]
	global_load_lds_dwordx4 v[230:231], off
	ds_read_b128 v[68:71], v2 offset:32768
	ds_read_b128 v[80:83], v2 offset:32896
	s_waitcnt lgkmcnt(0)
	v_mfma_f32_32x32x16_bf16 v[100:115], v[68:71], v[156:159], v[100:115]
	v_lshl_add_u64 v[230:231], s[52:53], 0, v[184:185]
	s_add_i32 m0, s100, 0x8400
	s_nop 0
	global_load_lds_dwordx4 v[230:231], off
	ds_read_b128 v[68:71], v2 offset:40960
	ds_read_b128 v[116:119], v2 offset:41088
	v_add_u32_e32 v2, s22, v205
	s_waitcnt lgkmcnt(0)
	v_mfma_f32_32x32x16_bf16 v[84:99], v[68:71], v[156:159], v[84:99]
	s_add_i32 m0, s100, 0x400
	s_nop 0
	global_load_lds_dwordx4 v[228:229], off
	ds_read_b128 v[68:71], v2 offset:32768
	ds_read_b128 v[120:123], v2 offset:32896
	s_waitcnt lgkmcnt(0)
	v_mfma_f32_32x32x16_bf16 v[100:115], v[68:71], v[152:155], v[100:115]
	ds_read_b128 v[68:71], v2 offset:40960
	ds_read_b128 v[124:127], v2 offset:41088
	v_add_u32_e32 v2, s22, v206
	s_lshl_b32 s22, 1, s76
	s_waitcnt lgkmcnt(0)
	v_mfma_f32_32x32x16_bf16 v[84:99], v[68:71], v[152:155], v[84:99]
	ds_read_b128 v[68:71], v2 offset:32768
	ds_read_b128 v[128:131], v2 offset:32896
	s_waitcnt lgkmcnt(0)
	v_mfma_f32_32x32x16_bf16 v[100:115], v[68:71], v[148:151], v[100:115]
	ds_read_b128 v[68:71], v2 offset:40960
	ds_read_b128 v[222:225], v2 offset:41088
	v_and_b32_e32 v2, s22, v219
	v_cmp_ne_u32_e32 vcc, 0, v2
	s_or_b64 s[12:13], s[12:13], vcc
	s_cmpk_gt_i32 s69, 0x7f
	s_waitcnt lgkmcnt(0)
	v_mfma_f32_32x32x16_bf16 v[84:99], v[68:71], v[148:151], v[84:99]
	v_mfma_f32_32x32x16_bf16 v[100:115], v[72:75], v[144:147], v[100:115]
	v_mfma_f32_32x32x16_bf16 v[84:99], v[76:79], v[144:147], v[84:99]
	v_mfma_f32_32x32x16_bf16 v[100:115], v[80:83], v[140:143], v[100:115]
	v_mfma_f32_32x32x16_bf16 v[84:99], v[116:119], v[140:143], v[84:99]
	v_mfma_f32_32x32x16_bf16 v[100:115], v[120:123], v[136:139], v[100:115]
	v_mfma_f32_32x32x16_bf16 v[84:99], v[124:127], v[136:139], v[84:99]
	v_mfma_f32_32x32x16_bf16 v[100:115], v[128:131], v[132:135], v[100:115]
	v_mfma_f32_32x32x16_bf16 v[84:99], v[222:225], v[132:135], v[84:99]
	s_cbranch_scc1 .LBB0_1594
	v_add_u32_e32 v117, s69, v220
	v_add_u32_e32 v2, 63, v117
	v_med3_i32 v68, v2, 32, v214
	v_lshl_add_u32 v68, v68, 2, s16
	v_add_u32_e32 v68, 0xffffff80, v68
	ds_read_b32 v116, v68
	v_cmp_lt_i32_e32 vcc, -1, v2
	s_and_b64 s[56:57], vcc, s[12:13]
	v_mov_b32_e32 v69, 0xff800000
	v_mov_b32_e32 v68, 0xff800000
	s_and_saveexec_b64 s[54:55], s[56:57]
	s_cbranch_execz .LBB0_1563
	v_min_u32_e32 v68, 0x80, v2
	v_lshl_add_u32 v68, v68, 2, 0
	v_add_u32_e32 v68, 0x14c00, v68
	ds_read_b32 v68, v68
	s_waitcnt lgkmcnt(0)
	v_add_f32_e32 v68, v100, v68

; template <bool MLA>
; __device__ __forceinline__ void attn_unit(char* lds, int h, int qb, const bf16_t* Qp, int ldq, const bf16_t* Kp, int ldk, const bf16_t* KRp, const bf16_t* Vp, int ldv,
;                                           unsigned char* Op, int ldo, const float* KMp, const float* rel_bias) {
;     ...
;         if (MLA || jb == qb) act = (kb <= qlo + 31) ? 1 : 0; else act = __any((int)((mysel >> jb) & 1u)) ? 1 : 0;
;         act = __builtin_amdgcn_readfirstlane(act);
;         if (act) {
;             f32x16 p0, p1;
; #pragma unroll
;             for (int r = 0; r < 16; ++r) { p0[r] = 0.f; p1[r] = 0.f; }
;             { const char* kn = lds + buf * SHM_KN; const char* kr = lds + buf * SHM_KR;
; #pragma unroll
;               for (int d0 = 0; d0 < 8; ++d0) { const char* ap = kn + kan[d0 & 3] + (d0 >> 2) * 128;
;                   const bf16x8 a0 = *(const bf16x8*)ap, a1 = *(const bf16x8*)(ap + 32 * 256);
;                   p0 = __builtin_amdgcn_mfma_f32_32x32x16_bf16(a0, qr[d0], p0, 0, 0, 0);
;                   p1 = __builtin_amdgcn_mfma_f32_32x32x16_bf16(a1, qr[d0], p1, 0, 0, 0); }
;               if constexpr (MLA) {
; #pragma unroll
;                   for (int d0 = 8; d0 < 12; ++d0) { const char* ap = kr + kar[d0 & 3];
;                       const bf16x8 a0 = *(const bf16x8*)ap, a1 = *(const bf16x8*)(ap + 32 * 128);
;                       p0 = __builtin_amdgcn_mfma_f32_32x32x16_bf16(a0, qr[d0], p0, 0, 0, 0);
;                       p1 = __builtin_amdgcn_mfma_f32_32x32x16_bf16(a1, qr[d0], p1, 0, 0, 0); } } }
;             const int dq = qpos - kb - 4 * hi;
;             if constexpr (MLA) {
;                 if (kb + 63 > qlo) {
; #pragma unroll
;                     for (int r = 0; r < 16; ++r) { const int d0 = dq - CROWC(r); if (d0 < 0) p0[r] = NEG; if (d0 < 32) p1[r] = NEG; } }
;             } else {
;                 const bool selq = (jb == qb) || (((mysel >> jb) & 1u) != 0u);
;                 if (q0 - (kb + 63) >= 128) { const float cb = bt_l[128];
; #pragma unroll
;                     for (int r = 0; r < 16; ++r) { p0[r] = selq ? p0[r] + cb : NEG; p1[r] = selq ? p1[r] + cb : NEG; } }
;                 else {
; #pragma unroll
;                     for (int r4 = 0; r4 < 4; ++r4) {
; #pragma unroll
;                         for (int rr = 0; rr < 4; ++rr) { const int r = r4 * 4 + rr; const int d0 = dq - CROWC(r), d1 = d0 - 32;
.LBB0_1603:
	s_bitcmp0_b32 s52, 0
	s_cbranch_scc1 .LBB0_1645
	s_lshl_b32 s22, s66, 14
	s_and_b32 s26, s22, 0x4000
	s_add_i32 s22, s26, 0
	v_add_u32_e32 v2, s22, v203
	ds_read_b128 v[68:71], v2 offset:32768
	ds_read_b128 v[72:75], v2 offset:32896
	s_mov_b64 s[52:53], -1
	s_waitcnt lgkmcnt(1)
	v_mfma_f32_32x32x16_bf16 v[100:115], v[68:71], v[160:163], 0
	ds_read_b128 v[68:71], v2 offset:40960
	ds_read_b128 v[76:79], v2 offset:41088
	v_add_u32_e32 v2, s22, v204
	s_waitcnt lgkmcnt(1)
	v_mfma_f32_32x32x16_bf16 v[84:99], v[68:71], v[160:163], 0
	ds_read_b128 v[68:71], v2 offset:32768
	ds_read_b128 v[80:83], v2 offset:32896
	s_waitcnt lgkmcnt(1)
	v_mfma_f32_32x32x16_bf16 v[100:115], v[68:71], v[156:159], v[100:115]
	ds_read_b128 v[68:71], v2 offset:40960
	ds_read_b128 v[116:119], v2 offset:41088
	v_add_u32_e32 v2, s22, v205
	s_waitcnt lgkmcnt(1)
	v_mfma_f32_32x32x16_bf16 v[84:99], v[68:71], v[156:159], v[84:99]
	ds_read_b128 v[68:71], v2 offset:32768
	ds_read_b128 v[120:123], v2 offset:32896
	s_waitcnt lgkmcnt(1)
	v_mfma_f32_32x32x16_bf16 v[100:115], v[68:71], v[152:155], v[100:115]
	ds_read_b128 v[68:71], v2 offset:40960
	ds_read_b128 v[124:127], v2 offset:41088
	v_add_u32_e32 v2, s22, v206
	s_lshl_b32 s22, 1, s27
	s_waitcnt lgkmcnt(1)
	v_mfma_f32_32x32x16_bf16 v[84:99], v[68:71], v[152:155], v[84:99]
	ds_read_b128 v[68:71], v2 offset:32768
	ds_read_b128 v[128:131], v2 offset:32896
	s_waitcnt lgkmcnt(1)
	v_mfma_f32_32x32x16_bf16 v[100:115], v[68:71], v[148:151], v[100:115]
	ds_read_b128 v[68:71], v2 offset:40960
	ds_read_b128 v[152:155], v2 offset:41088
	v_and_b32_e32 v2, s22, v219
	v_cmp_ne_u32_e32 vcc, 0, v2
	s_or_b64 s[12:13], s[12:13], vcc
	s_sub_i32 s22, s65, s54
	s_cmpk_gt_i32 s22, 0x7f
	s_waitcnt lgkmcnt(1)
	v_mfma_f32_32x32x16_bf16 v[84:99], v[68:71], v[148:151], v[84:99]
	v_mfma_f32_32x32x16_bf16 v[100:115], v[72:75], v[144:147], v[100:115]
	v_mfma_f32_32x32x16_bf16 v[84:99], v[76:79], v[144:147], v[84:99]
	v_mfma_f32_32x32x16_bf16 v[100:115], v[80:83], v[140:143], v[100:115]
	v_mfma_f32_32x32x16_bf16 v[84:99], v[116:119], v[140:143], v[84:99]
	v_mfma_f32_32x32x16_bf16 v[100:115], v[120:123], v[136:139], v[100:115]
	v_mfma_f32_32x32x16_bf16 v[84:99], v[124:127], v[136:139], v[84:99]
	v_mfma_f32_32x32x16_bf16 v[100:115], v[128:131], v[132:135], v[100:115]
	s_waitcnt lgkmcnt(0)
	v_mfma_f32_32x32x16_bf16 v[84:99], v[152:155], v[132:135], v[84:99]
	s_cbranch_scc1 .LBB0_1638
	v_subrev_u32_e32 v72, s54, v218
	v_sub_u32_e32 v2, v72, v165
	v_med3_i32 v68, v2, 32, v214
	v_lshl_add_u32 v68, v68, 2, s16
	v_add_u32_e32 v68, 0xffffff80, v68
	ds_read_b32 v116, v68
	v_cmp_lt_i32_e32 vcc, -1, v2
	s_and_b64 s[54:55], vcc, s[12:13]
	v_mov_b32_e32 v69, 0xff800000
	v_mov_b32_e32 v68, 0xff800000
	s_and_saveexec_b64 s[52:53], s[54:55]
	s_cbranch_execz .LBB0_1607
	v_min_u32_e32 v68, 0x80, v2
	v_lshl_add_u32 v68, v68, 2, 0
	v_add_u32_e32 v68, 0x14c00, v68
	ds_read_b32 v68, v68
	s_waitcnt lgkmcnt(0)
	v_add_f32_e32 v68, v100, v68
